# baseline (speedup 1.0000x reference)
.LBB3_14:
	s_and_b64 vcc, exec, s[4:5]
	s_cbranch_vccz .LBB3_29
	s_add_i32 s3, s2, 0xfffffc00
	s_and_b32 s8, s3, -8
	s_load_dwordx2 s[4:5], s[0:1], 0x8
	s_waitcnt lgkmcnt(0)
	s_load_dwordx2 s[6:7], s[14:15], s8 offset:0x0
	s_lshr_b32 s20, s3, 3
	s_and_saveexec_b64 s[8:9], s[10:11]
	s_cbranch_execz .LBB3_17
	s_waitcnt vmcnt(0)
	v_lshl_or_b32 v2, s20, 6, v0
	v_mov_b32_e32 v3, 0
	v_lshlrev_b64 v[2:3], 2, v[2:3]
	v_lshl_add_u64 v[4:5], s[16:17], 0, v[2:3]
	v_lshl_add_u64 v[2:3], s[18:19], 0, v[2:3]
	global_load_dword v49, v[4:5], off
	global_load_dword v50, v[2:3], off
	v_lshlrev_b32_e32 v51, 2, v0
	v_add_u32_e32 v51, 0x50, v51
.LBB3_17:
	s_or_b64 exec, exec, s[8:9]
	v_cmp_gt_u32_e32 vcc, 8, v0
	s_and_saveexec_b64 s[8:9], vcc
	s_cbranch_execz .LBB3_19
	v_mul_u32_u24_e32 v1, 0x70c, v0
	v_mov_b32_e32 v2, 0
	ds_write_b32 v1, v2
.LBB3_19:
	s_or_b64 exec, exec, s[8:9]
	s_lshl_b32 s22, s3, 3
	s_and_b32 s8, s20, 64
	s_and_b32 s9, s22, 56
	s_or_b32 s8, s8, s9
	s_waitcnt lgkmcnt(0)
	s_lshl_b32 s6, s6, 1
	s_lshl_b32 s23, s8, 7
	s_ashr_i32 s9, s6, 31
	s_add_u32 s8, s6, s23
	s_addc_u32 s9, s9, 0
	s_lshl_b64 s[8:9], s[8:9], 8
	s_add_u32 s6, s4, s8
	s_addc_u32 s8, s5, s9
	s_lshl_b32 s4, s7, 1
	s_ashr_i32 s5, s4, 31
	v_mul_u32_u24_e32 v1, 0x1112, v0
	s_lshl_b64 s[4:5], s[4:5], 1
	v_lshrrev_b32_e32 v34, 16, v1
	s_add_u32 s6, s6, s4
	v_mad_i32_i24 v8, v34, -15, v0
	v_mov_b32_e32 v1, 0x1c00
	v_mov_b32_e32 v4, 0x1d00
	v_cmp_lt_u32_e32 vcc, 14, v0
	s_addc_u32 s7, s8, s5
	v_lshlrev_b32_e32 v2, 1, v8
	v_cndmask_b32_e32 v4, v1, v4, vcc
	v_mov_b32_e32 v5, 0
	v_ashrrev_i32_e32 v3, 31, v2
	v_lshl_add_u64 v[6:7], s[6:7], 0, v[4:5]
	v_lshl_add_u64 v[6:7], v[2:3], 1, v[6:7]
	v_add_co_u32_e32 v6, vcc, 0x38000, v6
	s_movk_i32 s4, 0xff
	s_nop 0
	v_addc_co_u32_e32 v7, vcc, 0, v7, vcc
	global_load_dword v1, v[6:7], off
	v_lshlrev_b32_e32 v27, 2, v8
	v_cmp_gt_u32_e32 vcc, s4, v0
	v_mad_u32_u24 v26, v34, 60, v27
	s_and_saveexec_b64 s[4:5], vcc
	s_cbranch_execz .LBB3_21
	v_min_u32_e32 v4, 18, v34
	v_lshlrev_b32_e32 v4, 8, v4
	v_lshl_add_u64 v[8:9], s[6:7], 0, v[4:5]
	v_lshlrev_b64 v[6:7], 1, v[2:3]
	v_lshl_add_u64 v[2:3], v[8:9], 0, v[6:7]
	v_add_co_u32_e32 v2, vcc, 0x38000, v2
	v_add_u32_e32 v29, 0xcc, v34
	s_nop 0
	v_addc_co_u32_e32 v3, vcc, 0, v3, vcc
	v_min_u32_e32 v8, 0xef, v29
	global_load_dword v28, v[2:3], off offset:2816
	v_mul_lo_u16_e32 v2, 0x89, v8
	v_lshrrev_b16_e32 v9, 12, v2
	s_movk_i32 s8, 0xffe2
	v_mad_i32_i24 v8, v9, s8, v8
	v_lshlrev_b32_e32 v4, 15, v9
	v_ashrrev_i32_e32 v9, 31, v8
	v_lshl_add_u64 v[2:3], s[6:7], 0, v[4:5]
	v_lshlrev_b64 v[8:9], 8, v[8:9]
	v_lshl_add_u64 v[2:3], v[2:3], 0, v[8:9]
	v_add_u32_e32 v31, 0xbb, v34
	v_lshl_add_u64 v[2:3], v[2:3], 0, v[6:7]
	v_min_u32_e32 v8, 0xef, v31
	global_load_dword v30, v[2:3], off
	v_mul_lo_u16_e32 v2, 0x89, v8
	v_lshrrev_b16_e32 v9, 12, v2
	v_mad_i32_i24 v8, v9, s8, v8
	v_lshlrev_b32_e32 v4, 15, v9
	v_ashrrev_i32_e32 v9, 31, v8
	v_lshl_add_u64 v[2:3], s[6:7], 0, v[4:5]
	v_lshlrev_b64 v[8:9], 8, v[8:9]
	v_lshl_add_u64 v[2:3], v[2:3], 0, v[8:9]
	v_lshl_add_u64 v[2:3], v[2:3], 0, v[6:7]
	global_load_dword v32, v[2:3], off
	v_add_u32_e32 v2, 0xaa, v34
	v_mul_lo_u16_e32 v3, 0x89, v2
	v_lshrrev_b16_e32 v33, 12, v3
	v_mad_i32_i24 v2, v33, s8, v2
	v_lshlrev_b32_e32 v4, 15, v33
	v_ashrrev_i32_e32 v3, 31, v2
	v_lshl_add_u64 v[8:9], s[6:7], 0, v[4:5]
	v_lshlrev_b64 v[10:11], 8, v[2:3]
	v_lshl_add_u64 v[8:9], v[8:9], 0, v[10:11]
	v_lshl_add_u64 v[8:9], v[8:9], 0, v[6:7]
	global_load_dword v3, v[8:9], off
	v_add_u32_e32 v8, 0x99, v34
	v_mul_lo_u16_e32 v4, 0x89, v8
	v_lshrrev_b16_e32 v35, 12, v4
	v_mad_i32_i24 v8, v35, s8, v8
	v_lshlrev_b32_e32 v4, 15, v35
	v_ashrrev_i32_e32 v9, 31, v8
	v_lshl_add_u64 v[10:11], s[6:7], 0, v[4:5]
	v_lshlrev_b64 v[12:13], 8, v[8:9]
	v_lshl_add_u64 v[10:11], v[10:11], 0, v[12:13]
	v_lshl_add_u64 v[10:11], v[10:11], 0, v[6:7]
	global_load_dword v9, v[10:11], off
	v_add_u32_e32 v10, 0x88, v34
	v_mul_lo_u16_e32 v4, 0x89, v10
	v_lshrrev_b16_e32 v36, 12, v4
	v_mad_i32_i24 v10, v36, s8, v10
	v_lshlrev_b32_e32 v4, 15, v36
	v_ashrrev_i32_e32 v11, 31, v10
	v_lshl_add_u64 v[12:13], s[6:7], 0, v[4:5]
	v_lshlrev_b64 v[14:15], 8, v[10:11]
	v_lshl_add_u64 v[12:13], v[12:13], 0, v[14:15]
	v_lshl_add_u64 v[12:13], v[12:13], 0, v[6:7]
	global_load_dword v11, v[12:13], off
	v_add_u32_e32 v12, 0x77, v34
	v_mul_lo_u16_e32 v4, 0x89, v12
	v_lshrrev_b16_e32 v37, 12, v4
	v_mad_i32_i24 v12, v37, s8, v12
	v_lshlrev_b32_e32 v4, 15, v37
	v_ashrrev_i32_e32 v13, 31, v12
	v_lshl_add_u64 v[14:15], s[6:7], 0, v[4:5]
	v_lshlrev_b64 v[16:17], 8, v[12:13]
	v_lshl_add_u64 v[14:15], v[14:15], 0, v[16:17]
	v_lshl_add_u64 v[14:15], v[14:15], 0, v[6:7]
	global_load_dword v13, v[14:15], off
	v_add_u32_e32 v14, 0x66, v34
	v_mul_lo_u16_e32 v4, 0x89, v14
	v_lshrrev_b16_e32 v38, 12, v4
	v_mad_i32_i24 v14, v38, s8, v14
	v_lshlrev_b32_e32 v4, 15, v38
	v_ashrrev_i32_e32 v15, 31, v14
	v_lshl_add_u64 v[16:17], s[6:7], 0, v[4:5]
	v_lshlrev_b64 v[18:19], 8, v[14:15]
	v_lshl_add_u64 v[16:17], v[16:17], 0, v[18:19]
	v_lshl_add_u64 v[16:17], v[16:17], 0, v[6:7]
	global_load_dword v15, v[16:17], off
	v_add_u32_e32 v16, 0x55, v34
	v_mul_lo_u16_e32 v4, 0x89, v16
	v_lshrrev_b16_e32 v39, 12, v4
	v_mad_i32_i24 v16, v39, s8, v16
	v_lshlrev_b32_e32 v4, 15, v39
	v_ashrrev_i32_e32 v17, 31, v16
	v_lshl_add_u64 v[18:19], s[6:7], 0, v[4:5]
	v_lshlrev_b64 v[20:21], 8, v[16:17]
	v_lshl_add_u64 v[18:19], v[18:19], 0, v[20:21]
	v_lshl_add_u64 v[18:19], v[18:19], 0, v[6:7]
	global_load_dword v17, v[18:19], off
	v_add_u32_e32 v18, 0x44, v34
	v_mul_lo_u16_e32 v4, 0x89, v18
	v_lshrrev_b16_e32 v40, 12, v4
	v_mad_i32_i24 v18, v40, s8, v18
	v_lshlrev_b32_e32 v4, 15, v40
	v_ashrrev_i32_e32 v19, 31, v18
	v_lshl_add_u64 v[20:21], s[6:7], 0, v[4:5]
	v_lshlrev_b64 v[22:23], 8, v[18:19]
	v_lshl_add_u64 v[20:21], v[20:21], 0, v[22:23]
	v_lshl_add_u64 v[20:21], v[20:21], 0, v[6:7]
	global_load_dword v19, v[20:21], off
	v_add_u32_e32 v20, 51, v34
	v_mul_lo_u16_e32 v4, 0x89, v20
	v_lshrrev_b16_e32 v41, 12, v4
	v_mad_i32_i24 v20, v41, s8, v20
	v_lshlrev_b32_e32 v4, 15, v41
	v_ashrrev_i32_e32 v21, 31, v20
	v_lshl_add_u64 v[22:23], s[6:7], 0, v[4:5]
	v_lshlrev_b64 v[24:25], 8, v[20:21]
	v_lshl_add_u64 v[22:23], v[22:23], 0, v[24:25]
	v_lshl_add_u64 v[22:23], v[22:23], 0, v[6:7]
	global_load_dword v21, v[22:23], off
	v_add_u32_e32 v22, 34, v34
	v_mul_lo_u16_e32 v4, 0x89, v22
	v_lshrrev_b16_e32 v42, 12, v4
	v_mad_i32_i24 v22, v42, s8, v22
	v_lshlrev_b32_e32 v4, 15, v42
	v_ashrrev_i32_e32 v23, 31, v22
	v_lshl_add_u64 v[24:25], s[6:7], 0, v[4:5]
	v_lshlrev_b64 v[44:45], 8, v[22:23]
	v_lshl_add_u64 v[24:25], v[24:25], 0, v[44:45]
	v_lshl_add_u64 v[24:25], v[24:25], 0, v[6:7]
	global_load_dword v23, v[24:25], off
	v_add_u32_e32 v24, 17, v34
	v_mul_lo_u16_e32 v4, 0x89, v24
	v_lshrrev_b16_e32 v43, 12, v4
	v_mad_i32_i24 v24, v43, s8, v24
	s_movk_i32 s9, 0x89
	v_lshlrev_b32_e32 v4, 15, v43
	v_ashrrev_i32_e32 v25, 31, v24
	v_lshl_add_u64 v[44:45], s[6:7], 0, v[4:5]
	v_lshlrev_b64 v[46:47], 8, v[24:25]
	v_mul_lo_u16_sdwa v4, v34, s9 dst_sel:DWORD dst_unused:UNUSED_PAD src0_sel:BYTE_0 src1_sel:DWORD
	v_lshl_add_u64 v[44:45], v[44:45], 0, v[46:47]
	v_lshrrev_b16_e32 v48, 12, v4
	v_lshl_add_u64 v[44:45], v[44:45], 0, v[6:7]
	v_lshlrev_b32_e32 v4, 15, v48
	global_load_dword v25, v[44:45], off
	v_lshl_add_u64 v[44:45], s[6:7], 0, v[4:5]
	v_mad_i32_i24 v4, v48, s8, v34
	v_ashrrev_i32_e32 v5, 31, v4
	v_lshlrev_b64 v[46:47], 8, v[4:5]
	v_lshl_add_u64 v[44:45], v[44:45], 0, v[46:47]
	v_lshl_add_u64 v[6:7], v[44:45], 0, v[6:7]
	global_load_dword v5, v[6:7], off
	v_mul_u32_u24_e32 v6, 0x70c, v48
	v_mul_lo_u32 v4, v4, 60
	v_add3_u32 v4, v6, v4, v27
	v_mul_lo_u32 v2, v2, 60
	s_waitcnt vmcnt(0)
	ds_write_b32 v4, v5 offset:4
	v_mul_u32_u24_e32 v4, 0x70c, v43
	v_mul_lo_u32 v5, v24, 60
	v_add3_u32 v4, v4, v5, v27
	ds_write_b32 v4, v25 offset:4
	v_mul_u32_u24_e32 v4, 0x70c, v42
	v_mul_lo_u32 v5, v22, 60
	v_add3_u32 v4, v4, v5, v27
	ds_write_b32 v4, v23 offset:4
	v_mul_u32_u24_e32 v4, 0x70c, v41
	v_mul_lo_u32 v5, v20, 60
	v_add3_u32 v4, v4, v5, v27
	ds_write_b32 v4, v21 offset:4
	v_mul_u32_u24_e32 v4, 0x70c, v40
	v_mul_lo_u32 v5, v18, 60
	v_add3_u32 v4, v4, v5, v27
	ds_write_b32 v4, v19 offset:4
	v_mul_u32_u24_e32 v4, 0x70c, v39
	v_mul_lo_u32 v5, v16, 60
	v_add3_u32 v4, v4, v5, v27
	ds_write_b32 v4, v17 offset:4
	v_mul_u32_u24_e32 v4, 0x70c, v38
	v_mul_lo_u32 v5, v14, 60
	v_add3_u32 v4, v4, v5, v27
	ds_write_b32 v4, v15 offset:4
	v_mul_u32_u24_e32 v4, 0x70c, v37
	v_mul_lo_u32 v5, v12, 60
	v_add3_u32 v4, v4, v5, v27
	ds_write_b32 v4, v13 offset:4
	v_mul_u32_u24_e32 v4, 0x70c, v36
	v_mul_lo_u32 v5, v10, 60
	v_add3_u32 v4, v4, v5, v27
	ds_write_b32 v4, v11 offset:4
	v_mul_u32_u24_e32 v4, 0x70c, v35
	v_mul_lo_u32 v5, v8, 60
	v_add3_u32 v4, v4, v5, v27
	ds_write_b32 v4, v9 offset:4
	v_mul_u32_u24_e32 v4, 0x70c, v33
	v_add3_u32 v2, v4, v2, v27
	ds_write_b32 v2, v3 offset:4
	v_mul_lo_u16_e32 v2, 0x89, v31
	v_lshrrev_b16_e32 v2, 12, v2
	v_mad_i32_i24 v3, v2, s8, v31
	v_mul_u32_u24_e32 v2, 0x70c, v2
	v_mul_lo_u32 v3, v3, 60
	v_add3_u32 v2, v2, v3, v27
	ds_write_b32 v2, v32 offset:4
	v_mul_lo_u16_e32 v2, 0x89, v29
	v_lshrrev_b16_e32 v2, 12, v2
	v_mad_i32_i24 v3, v2, s8, v29
	v_mul_u32_u24_e32 v2, 0x70c, v2
	v_mul_lo_u32 v3, v3, 60
	v_add3_u32 v2, v2, v3, v27
	ds_write_b32 v2, v30 offset:4
	ds_write_b32 v26, v28 offset:13292

.LBB3_23:
	s_or_b64 exec, exec, s[4:5]
	s_and_saveexec_b64 s[4:5], s[10:11]
	s_waitcnt vmcnt(0)
	ds_write2st64_b32 v51, v49, v50 offset0:70 offset1:71
	s_or_b64 exec, exec, s[4:5]
	v_and_b32_e32 v6, 7, v0
	s_waitcnt vmcnt(0)
	v_lshrrev_b32_e32 v1, 3, v0
	v_add_u32_e32 v15, 1, v6
	v_bfe_u32 v3, v1, 1, 3
	v_min_u32_e32 v2, 7, v15
	v_add_u32_e32 v9, 1, v3
	v_lshlrev_b32_e32 v11, 2, v2
	v_add_u32_e32 v2, -1, v6
	v_min_u32_e32 v4, 7, v9
	v_mov_b32_e32 v5, 0x4650
	v_max_i32_e32 v10, 0, v2
	v_lshl_add_u32 v8, v4, 5, v5
	v_lshlrev_b32_e32 v4, 2, v6
	v_lshlrev_b32_e32 v17, 2, v10
	v_lshl_add_u32 v10, v3, 5, v5
	v_add_u32_e32 v14, v10, v11
	v_add_u32_e32 v16, v10, v4
	v_add_u32_e32 v18, v10, v17
	v_add_u32_e32 v10, -1, v3
	v_max_i32_e32 v19, 0, v10
	v_lshl_add_u32 v19, v19, 5, v5
	v_add_u32_e32 v12, v8, v11
	v_add_u32_e32 v13, v8, v4
	v_add_u32_e32 v8, v8, v17
	v_add_u32_e32 v5, v19, v11
	s_waitcnt lgkmcnt(0)
	s_barrier
	v_bfe_u32 v1, v0, 3, 1
	v_add_u32_e32 v11, v19, v4
	ds_read_b32 v12, v12
	ds_read_b32 v13, v13
	ds_read_b32 v20, v8
	ds_read_b32 v14, v14
	ds_read_b32 v8, v16
	ds_read_b32 v16, v18
	ds_read_b32 v18, v5
	ds_read_b32 v21, v11
	s_waitcnt lgkmcnt(7)
	v_ashrrev_i32_e32 v5, 3, v12
	s_mov_b32 s24, 0x7ffffffe
	v_and_or_b32 v5, v5, s24, v1
	v_lshlrev_b32_e32 v11, 1, v12
	v_mul_lo_u32 v5, v5, 30
	v_and_b32_e32 v11, 30, v11
	v_add3_u32 v5, v11, v5, 2
	v_or_b32_e32 v11, v9, v15
	v_cmp_gt_u32_e32 vcc, 8, v11
	s_waitcnt lgkmcnt(6)
	v_ashrrev_i32_e32 v11, 3, v13
	v_and_or_b32 v11, v11, s24, v1
	v_lshlrev_b32_e32 v12, 1, v13
	v_mul_lo_u32 v11, v11, 30
	v_and_b32_e32 v12, 30, v12
	v_add3_u32 v11, v12, v11, 4
	s_waitcnt lgkmcnt(5)
	v_ashrrev_i32_e32 v12, 3, v20
	v_and_or_b32 v12, v12, s24, v1
	v_lshlrev_b32_e32 v13, 1, v20
	v_mul_lo_u32 v12, v12, 30
	v_and_b32_e32 v13, 30, v13
	v_or_b32_e32 v9, v9, v2
	v_cndmask_b32_e32 v5, 0, v5, vcc
	v_add3_u32 v12, v13, v12, 6
	v_cmp_gt_u32_e32 vcc, 8, v9
	s_waitcnt lgkmcnt(4)
	v_ashrrev_i32_e32 v9, 3, v14
	v_lshlrev_b32_e32 v13, 1, v14
	s_waitcnt lgkmcnt(2)
	v_ashrrev_i32_e32 v14, 3, v16
	v_and_or_b32 v14, v14, s24, v1
	v_lshlrev_b32_e32 v16, 1, v16
	v_mul_lo_u32 v14, v14, 30
	v_and_b32_e32 v16, 30, v16
	s_movk_i32 s6, 0x42
	v_add3_u32 v14, v14, v16, s6
	s_waitcnt lgkmcnt(1)
	v_ashrrev_i32_e32 v16, 3, v18
	v_cmp_eq_u32_e64 s[4:5], 7, v3
	v_and_or_b32 v16, v16, s24, v1
	v_lshlrev_b32_e32 v18, 1, v18
	v_cndmask_b32_e64 v11, v11, 0, s[4:5]
	v_cndmask_b32_e64 v24, 2, 1, s[4:5]
	v_mul_lo_u32 v16, v16, 30
	v_and_b32_e32 v18, 30, v18
	s_movk_i32 s4, 0x7a
	v_or_b32_e32 v15, v10, v15
	v_add3_u32 v16, v16, v18, s4
	v_cmp_gt_u32_e64 s[4:5], 8, v15
	s_waitcnt lgkmcnt(0)
	v_lshlrev_b32_e32 v18, 1, v21
	v_and_b32_e32 v18, 30, v18
	v_cndmask_b32_e64 v15, 0, v16, s[4:5]
	v_ashrrev_i32_e32 v16, 3, v21
	v_and_or_b32 v16, v16, s24, v1
	v_mul_lo_u32 v16, v16, 30
	s_movk_i32 s4, 0x7c
	v_add3_u32 v16, v16, v18, s4
	v_cvt_f32_ubyte0_e32 v18, v1
	v_add_f32_e32 v18, 0.5, v18
	v_fma_f32 v25, v18, 0.5, -0.5
	v_cmp_gt_f32_e64 s[8:9], 0, v25
	v_add_u32_e32 v17, v19, v17
	v_sub_u32_e64 v19, v6, 1 clamp
	v_subbrev_co_u32_e64 v18, s[10:11], 0, v3, s[8:9]
	v_cmp_ngt_f32_e64 s[10:11], 0, v25
	v_max_i32_e32 v18, 0, v18
	v_min_u32_e32 v20, 6, v6
	v_addc_co_u32_e64 v3, s[10:11], 0, v3, s[10:11]
	v_min_u32_e32 v3, 7, v3
	v_mov_b32_e32 v21, 0x4750
	v_lshl_add_u32 v18, v18, 5, v21
	v_lshlrev_b32_e32 v19, 2, v19
	v_lshl_add_u32 v3, v3, 5, v21
	v_lshlrev_b32_e32 v20, 2, v20
	v_add_u32_e32 v22, v18, v19
	v_add_u32_e32 v19, v3, v19
	v_add_u32_e32 v21, v18, v4
	v_add_u32_e32 v4, v3, v4
	v_add_u32_e32 v3, v3, v20
	v_and_or_b32 v9, v9, s24, v1
	v_add_u32_e32 v26, v18, v20
	ds_read_b32 v17, v17
	ds_read_b32 v18, v22
	ds_read_b32 v20, v19
	ds_read_b32 v22, v21
	ds_read_b32 v23, v4
	ds_read_b32 v19, v26 offset:4
	ds_read_b32 v21, v3 offset:4
	s_waitcnt lgkmcnt(6)
	v_ashrrev_i32_e32 v3, 3, v17
	v_cndmask_b32_e32 v12, 0, v12, vcc
	v_mul_lo_u32 v9, v9, 30
	v_and_b32_e32 v13, 30, v13
	v_cmp_eq_u32_e32 vcc, 7, v6
	v_and_or_b32 v3, v3, s24, v1
	v_lshlrev_b32_e32 v4, 1, v17
	v_add3_u32 v9, v9, v13, 62
	v_cmp_gt_u32_e64 s[6:7], 8, v2
	v_cmp_gt_u32_e64 s[4:5], 8, v10
	v_mul_lo_u32 v3, v3, 30
	v_and_b32_e32 v4, 30, v4
	s_movk_i32 s10, 0x7e
	v_cndmask_b32_e64 v17, 2, 1, vcc
	v_cndmask_b32_e64 v13, v9, 0, vcc
	v_cndmask_b32_e64 v16, 0, v16, s[4:5]
	v_add3_u32 v3, v3, v4, s10
	v_addc_co_u32_e64 v4, s[4:5], 0, v24, s[4:5]
	v_addc_co_u32_e64 v17, vcc, 0, v17, s[6:7]
	v_mul_u32_u24_e32 v4, v4, v17
	v_cvt_f32_ubyte0_e32 v4, v4
	v_div_scale_f32 v17, s[4:5], v4, v4, 1.0
	v_rcp_f32_e32 v24, v17
	v_or_b32_e32 v2, v10, v2
	v_cmp_gt_u32_e32 vcc, 8, v2
	s_load_dwordx2 s[12:13], s[0:1], 0x38
	v_fma_f32 v2, -v17, v24, 1.0
	v_cndmask_b32_e32 v26, 0, v3, vcc
	v_fmac_f32_e32 v24, v2, v24
	v_div_scale_f32 v2, vcc, 1.0, v4, 1.0
	v_mul_f32_e32 v3, v2, v24
	v_fma_f32 v10, -v17, v3, v2
	v_fmac_f32_e32 v3, v10, v24
	v_fma_f32 v2, -v17, v3, v2
	v_div_fmas_f32 v2, v2, v24, v3
	v_add_f32_e32 v3, 1.0, v25
	v_cndmask_b32_e64 v25, v25, v3, s[8:9]
	v_sub_f32_e32 v24, 1.0, v25
	s_waitcnt lgkmcnt(0)
	v_pk_mul_f32 v[22:23], v[24:25], v[22:23]
	v_mov_b32_e32 v10, v25
	v_add_f32_e32 v3, v22, v23
	v_pk_mul_f32 v[20:21], v[10:11], v[20:21] op_sel_hi:[0,1]
	v_div_fixup_f32 v2, v2, v4, 1.0
	v_mul_f32_e32 v4, 0x3f400000, v3
	v_pk_fma_f32 v[18:19], v[24:25], v[18:19], v[20:21] op_sel_hi:[0,1,1]
	s_mov_b32 s4, 0x3e800000
	v_pk_fma_f32 v[18:19], v[18:19], s[4:5], v[4:5] op_sel_hi:[1,0,0]
	v_cndmask_b32_e64 v14, 0, v14, s[6:7]
	v_pk_mul_f32 v[2:3], v[2:3], v[18:19] op_sel_hi:[0,1]
	s_lshr_b32 s4, s2, 2
	v_lshrrev_b32_e32 v19, 7, v0
	v_bfe_u32 v7, v0, 3, 4
	s_mov_b32 s21, 0
	v_ashrrev_i32_e32 v9, 3, v8
	s_and_b32 s8, s4, 0x70
	v_xor_b32_e32 v18, 7, v19
	s_mov_b64 s[6:7], 0
	v_lshlrev_b32_e32 v10, 1, v5
	v_lshlrev_b32_e32 v11, 1, v11
	v_lshlrev_b32_e32 v12, 1, v12
	v_lshlrev_b32_e32 v13, 1, v13
	v_lshlrev_b32_e32 v14, 1, v14
	v_lshlrev_b32_e32 v15, 1, v15
	v_lshlrev_b32_e32 v16, 1, v16
	v_lshlrev_b32_e32 v17, 1, v26
	s_and_saveexec_b64 s[4:5], s[6:7]
	s_cbranch_execz .LBB3_25
	s_mov_b32 s6, 0x3ffffffe
	v_and_or_b32 v4, v9, s6, v1
	s_or_b32 s6, s8, s23
	v_mul_lo_u32 v22, v4, 60
	v_or_b32_e32 v4, s6, v7
	v_lshlrev_b32_e32 v4, 9, v4
	v_mov_b32_e32 v5, 0
	s_lshl_b32 s6, s20, 6
	v_lshlrev_b32_e32 v23, 2, v8
	v_lshl_add_u64 v[20:21], s[12:13], 0, v[4:5]
	s_and_b32 s20, s6, 0x1c0
	s_movk_i32 s6, 0x70c
	v_mul_u32_u24_e32 v4, 0x70c, v19
	v_and_b32_e32 v23, 60, v23
	v_add3_u32 v4, v4, v23, v22
	v_mad_u32_u24 v22, v19, s6, v10
	v_mad_u32_u24 v23, v19, s6, v11
	v_mad_u32_u24 v24, v19, s6, v12
	v_mad_u32_u24 v25, v19, s6, v13
	v_mad_u32_u24 v26, v19, s6, v14
	v_mad_u32_u24 v27, v19, s6, v15
	v_mad_u32_u24 v28, v19, s6, v16
	ds_read_b32 v22, v22
	ds_read_b32 v23, v23
	ds_read_b32 v24, v24
	ds_read_b32 v25, v25
	ds_read_b32 v26, v26
	ds_read_b32 v27, v27
	ds_read_b32 v28, v28
	ds_read_b32 v4, v4 offset:128
	s_waitcnt lgkmcnt(6)
	v_pk_add_f16 v22, v22, v23
	v_mad_u32_u24 v23, v19, s6, v17
	s_waitcnt lgkmcnt(5)
	v_pk_add_f16 v22, v22, v24
	ds_read_b32 v23, v23
	s_waitcnt lgkmcnt(5)
	v_pk_add_f16 v22, v22, v25
	v_lshl_add_u64 v[20:21], v[20:21], 0, s[20:21]
	s_waitcnt lgkmcnt(1)
	v_pk_add_f16 v4, v22, v4
	s_nop 0
	v_pk_add_f16 v4, v4, v26
	s_nop 0
	v_pk_add_f16 v4, v4, v27
	s_nop 0
	v_pk_add_f16 v4, v4, v28
	s_waitcnt lgkmcnt(0)
	v_pk_add_f16 v4, v4, v23
	s_nop 0
	v_cvt_f32_f16_e32 v22, v4
	v_cvt_f32_f16_sdwa v23, v4 dst_sel:DWORD dst_unused:UNUSED_PAD src0_sel:WORD_1
	v_lshlrev_b32_e32 v4, 3, v6
	v_lshl_add_u64 v[20:21], v[20:21], 0, v[4:5]
	v_lshlrev_b32_e32 v4, 16, v19
	v_pk_mul_f32 v[22:23], v[2:3], v[22:23]
	v_lshl_add_u64 v[4:5], v[20:21], 0, v[4:5]
	v_or_b32_e32 v19, 2, v19
	global_store_dwordx2 v[4:5], v[22:23], off nt
